# v2 + phase-0 silu(c) staging loop issues its 8 loads together
# speedup vs baseline: 1.0002x; 1.0002x over previous
; #define LAS __attribute__((address_space(3)))
; __device__ __forceinline__ float silu_f(float v) { return v / (1.f + expf(-v)); }
; __device__ __forceinline__ void phase_prologue(const Args& a, LAS unsigned char* lds) {
;     ...
;     if (blk < 192) {
;         LAS float* cact = (LAS float*)lds; LAS float* red = (LAS float*)(lds + 16384);
;         for (int i = tid; i < 4096; i += 512) cact[i] = silu_f(a.c[i]);
;         __syncthreads();
.LBB0_8:
	global_load_dword v14, v[4:5], off
	v_lshl_add_u64 v[4:5], v[4:5], 0, s[4:5]
	global_load_dword v15, v[4:5], off
	v_lshl_add_u64 v[4:5], v[4:5], 0, s[4:5]
	global_load_dword v16, v[4:5], off
	v_lshl_add_u64 v[4:5], v[4:5], 0, s[4:5]
	global_load_dword v17, v[4:5], off
	v_lshl_add_u64 v[4:5], v[4:5], 0, s[4:5]
	global_load_dword v18, v[4:5], off
	v_lshl_add_u64 v[4:5], v[4:5], 0, s[4:5]
	global_load_dword v19, v[4:5], off
	v_lshl_add_u64 v[4:5], v[4:5], 0, s[4:5]
	global_load_dword v20, v[4:5], off
	v_lshl_add_u64 v[4:5], v[4:5], 0, s[4:5]
	global_load_dword v21, v[4:5], off
	s_waitcnt vmcnt(7)
	v_mov_b32_e32 v7, v14
	v_mul_f32_e32 v8, 0xbfb8aa3b, v7
	v_rndne_f32_e32 v9, v8
	v_fma_f32 v10, v7, s3, -v8
	v_sub_f32_e32 v8, v8, v9
	v_fmac_f32_e32 v10, 0xb2a5705f, v7
	v_add_f32_e32 v8, v8, v10
	v_cvt_i32_f32_e32 v9, v9
	v_exp_f32_e32 v8, v8
	v_cmp_nlt_f32_e32 vcc, s6, v7
	v_ldexp_f32 v8, v8, v9
	s_nop 0
	v_cndmask_b32_e32 v8, 0, v8, vcc
	v_cmp_ngt_f32_e32 vcc, s7, v7
	s_nop 1
	v_cndmask_b32_e32 v8, v3, v8, vcc
	v_add_f32_e32 v8, 1.0, v8
	v_div_scale_f32 v9, s[10:11], v8, v8, v7
	v_rcp_f32_e32 v10, v9
	v_div_scale_f32 v11, vcc, v7, v8, v7
	v_fma_f32 v12, -v9, v10, 1.0
	v_fmac_f32_e32 v10, v12, v10
	v_mul_f32_e32 v12, v11, v10
	v_fma_f32 v13, -v9, v12, v11
	v_fmac_f32_e32 v12, v13, v10
	v_fma_f32 v9, -v9, v12, v11
	v_div_fmas_f32 v9, v9, v10, v12
	v_div_fixup_f32 v7, v9, v8, v7
	ds_write_b32 v6, v7
	v_add_u32_e32 v6, 0x800, v6
	s_waitcnt vmcnt(6)
	v_mov_b32_e32 v7, v15
	v_mul_f32_e32 v8, 0xbfb8aa3b, v7
	v_rndne_f32_e32 v9, v8
	v_fma_f32 v10, v7, s3, -v8
	v_sub_f32_e32 v8, v8, v9
	v_fmac_f32_e32 v10, 0xb2a5705f, v7
	v_add_f32_e32 v8, v8, v10
	v_cvt_i32_f32_e32 v9, v9
	v_exp_f32_e32 v8, v8
	v_cmp_nlt_f32_e32 vcc, s6, v7
	v_ldexp_f32 v8, v8, v9
	s_nop 0
	v_cndmask_b32_e32 v8, 0, v8, vcc
	v_cmp_ngt_f32_e32 vcc, s7, v7
	s_nop 1
	v_cndmask_b32_e32 v8, v3, v8, vcc
	v_add_f32_e32 v8, 1.0, v8
	v_div_scale_f32 v9, s[10:11], v8, v8, v7
	v_rcp_f32_e32 v10, v9
	v_div_scale_f32 v11, vcc, v7, v8, v7
	v_fma_f32 v12, -v9, v10, 1.0
	v_fmac_f32_e32 v10, v12, v10
	v_mul_f32_e32 v12, v11, v10
	v_fma_f32 v13, -v9, v12, v11
	v_fmac_f32_e32 v12, v13, v10
	v_fma_f32 v9, -v9, v12, v11
	v_div_fmas_f32 v9, v9, v10, v12
	v_div_fixup_f32 v7, v9, v8, v7
	ds_write_b32 v6, v7
	v_add_u32_e32 v6, 0x800, v6
	s_waitcnt vmcnt(5)
	v_mov_b32_e32 v7, v16
	v_mul_f32_e32 v8, 0xbfb8aa3b, v7
	v_rndne_f32_e32 v9, v8
	v_fma_f32 v10, v7, s3, -v8
	v_sub_f32_e32 v8, v8, v9
	v_fmac_f32_e32 v10, 0xb2a5705f, v7
	v_add_f32_e32 v8, v8, v10
	v_cvt_i32_f32_e32 v9, v9
	v_exp_f32_e32 v8, v8
	v_cmp_nlt_f32_e32 vcc, s6, v7
	v_ldexp_f32 v8, v8, v9
	s_nop 0
	v_cndmask_b32_e32 v8, 0, v8, vcc
	v_cmp_ngt_f32_e32 vcc, s7, v7
	s_nop 1
	v_cndmask_b32_e32 v8, v3, v8, vcc
	v_add_f32_e32 v8, 1.0, v8
	v_div_scale_f32 v9, s[10:11], v8, v8, v7
	v_rcp_f32_e32 v10, v9
	v_div_scale_f32 v11, vcc, v7, v8, v7
	v_fma_f32 v12, -v9, v10, 1.0
	v_fmac_f32_e32 v10, v12, v10
	v_mul_f32_e32 v12, v11, v10
	v_fma_f32 v13, -v9, v12, v11
	v_fmac_f32_e32 v12, v13, v10
	v_fma_f32 v9, -v9, v12, v11
	v_div_fmas_f32 v9, v9, v10, v12
	v_div_fixup_f32 v7, v9, v8, v7
	ds_write_b32 v6, v7
	v_add_u32_e32 v6, 0x800, v6
	s_waitcnt vmcnt(4)
	v_mov_b32_e32 v7, v17
	v_mul_f32_e32 v8, 0xbfb8aa3b, v7
	v_rndne_f32_e32 v9, v8
	v_fma_f32 v10, v7, s3, -v8
	v_sub_f32_e32 v8, v8, v9
	v_fmac_f32_e32 v10, 0xb2a5705f, v7
	v_add_f32_e32 v8, v8, v10
	v_cvt_i32_f32_e32 v9, v9
	v_exp_f32_e32 v8, v8
	v_cmp_nlt_f32_e32 vcc, s6, v7
	v_ldexp_f32 v8, v8, v9
	s_nop 0
	v_cndmask_b32_e32 v8, 0, v8, vcc
	v_cmp_ngt_f32_e32 vcc, s7, v7
	s_nop 1
	v_cndmask_b32_e32 v8, v3, v8, vcc
	v_add_f32_e32 v8, 1.0, v8
	v_div_scale_f32 v9, s[10:11], v8, v8, v7
	v_rcp_f32_e32 v10, v9
	v_div_scale_f32 v11, vcc, v7, v8, v7
	v_fma_f32 v12, -v9, v10, 1.0
	v_fmac_f32_e32 v10, v12, v10
	v_mul_f32_e32 v12, v11, v10
	v_fma_f32 v13, -v9, v12, v11
	v_fmac_f32_e32 v12, v13, v10
	v_fma_f32 v9, -v9, v12, v11
	v_div_fmas_f32 v9, v9, v10, v12
	v_div_fixup_f32 v7, v9, v8, v7
	ds_write_b32 v6, v7
	v_add_u32_e32 v6, 0x800, v6
	s_waitcnt vmcnt(3)
	v_mov_b32_e32 v7, v18
	v_mul_f32_e32 v8, 0xbfb8aa3b, v7
	v_rndne_f32_e32 v9, v8
	v_fma_f32 v10, v7, s3, -v8
	v_sub_f32_e32 v8, v8, v9
	v_fmac_f32_e32 v10, 0xb2a5705f, v7
	v_add_f32_e32 v8, v8, v10
	v_cvt_i32_f32_e32 v9, v9
	v_exp_f32_e32 v8, v8
	v_cmp_nlt_f32_e32 vcc, s6, v7
	v_ldexp_f32 v8, v8, v9
	s_nop 0
	v_cndmask_b32_e32 v8, 0, v8, vcc
	v_cmp_ngt_f32_e32 vcc, s7, v7
	s_nop 1
	v_cndmask_b32_e32 v8, v3, v8, vcc
	v_add_f32_e32 v8, 1.0, v8
	v_div_scale_f32 v9, s[10:11], v8, v8, v7
	v_rcp_f32_e32 v10, v9
	v_div_scale_f32 v11, vcc, v7, v8, v7
	v_fma_f32 v12, -v9, v10, 1.0
	v_fmac_f32_e32 v10, v12, v10
	v_mul_f32_e32 v12, v11, v10
	v_fma_f32 v13, -v9, v12, v11
	v_fmac_f32_e32 v12, v13, v10
	v_fma_f32 v9, -v9, v12, v11
	v_div_fmas_f32 v9, v9, v10, v12
	v_div_fixup_f32 v7, v9, v8, v7
	ds_write_b32 v6, v7
	v_add_u32_e32 v6, 0x800, v6
	s_waitcnt vmcnt(2)
; __device__ __forceinline__ float silu_f(float v) { return v / (1.f + expf(-v)); }
; __device__ __forceinline__ void phase_prologue(const Args& a, LAS unsigned char* lds) {
;     ...
;         for (int i = tid; i < 4096; i += 512) cact[i] = silu_f(a.c[i]);
;         __syncthreads();
;         float* mod = (float*)(a.ws + WS_MOD);
;         for (int job = blk; job < 192; job += G) {
;             const int cg = job % 48, kg = job / 48, w = tid >> 6, lane = tid & 63;
;             const float* wp = a.w_ada + (size_t)(kg * 512 + w) * 12288 + cg * 256 + lane * 4;
;             f32x4 a0 = {0.f, 0.f, 0.f, 0.f}, a1 = {0.f, 0.f, 0.f, 0.f};
; #pragma unroll 16
;             for (int i = 0; i < 64; ++i) { const int k = kg * 512 + w + 8 * i; const f32x4 wv = *(const f32x4*)(wp + (size_t)(8 * i) * 12288); a0 += wv * cact[k]; a1 += wv * cact[2048 + k]; }
	v_mov_b32_e32 v7, v19
	v_mul_f32_e32 v8, 0xbfb8aa3b, v7
	v_rndne_f32_e32 v9, v8
	v_fma_f32 v10, v7, s3, -v8
	v_sub_f32_e32 v8, v8, v9
	v_fmac_f32_e32 v10, 0xb2a5705f, v7
	v_add_f32_e32 v8, v8, v10
	v_cvt_i32_f32_e32 v9, v9
	v_exp_f32_e32 v8, v8
	v_cmp_nlt_f32_e32 vcc, s6, v7
	v_ldexp_f32 v8, v8, v9
	s_nop 0
	v_cndmask_b32_e32 v8, 0, v8, vcc
	v_cmp_ngt_f32_e32 vcc, s7, v7
	s_nop 1
	v_cndmask_b32_e32 v8, v3, v8, vcc
	v_add_f32_e32 v8, 1.0, v8
	v_div_scale_f32 v9, s[10:11], v8, v8, v7
	v_rcp_f32_e32 v10, v9
	v_div_scale_f32 v11, vcc, v7, v8, v7
	v_fma_f32 v12, -v9, v10, 1.0
	v_fmac_f32_e32 v10, v12, v10
	v_mul_f32_e32 v12, v11, v10
	v_fma_f32 v13, -v9, v12, v11
	v_fmac_f32_e32 v12, v13, v10
	v_fma_f32 v9, -v9, v12, v11
	v_div_fmas_f32 v9, v9, v10, v12
	v_div_fixup_f32 v7, v9, v8, v7
	ds_write_b32 v6, v7
	v_add_u32_e32 v6, 0x800, v6
	s_waitcnt vmcnt(1)
	v_mov_b32_e32 v7, v20
	v_mul_f32_e32 v8, 0xbfb8aa3b, v7
	v_rndne_f32_e32 v9, v8
	v_fma_f32 v10, v7, s3, -v8
	v_sub_f32_e32 v8, v8, v9
	v_fmac_f32_e32 v10, 0xb2a5705f, v7
	v_add_f32_e32 v8, v8, v10
	v_cvt_i32_f32_e32 v9, v9
	v_exp_f32_e32 v8, v8
	v_cmp_nlt_f32_e32 vcc, s6, v7
	v_ldexp_f32 v8, v8, v9
	s_nop 0
	v_cndmask_b32_e32 v8, 0, v8, vcc
	v_cmp_ngt_f32_e32 vcc, s7, v7
	s_nop 1
	v_cndmask_b32_e32 v8, v3, v8, vcc
	v_add_f32_e32 v8, 1.0, v8
	v_div_scale_f32 v9, s[10:11], v8, v8, v7
	v_rcp_f32_e32 v10, v9
	v_div_scale_f32 v11, vcc, v7, v8, v7
	v_fma_f32 v12, -v9, v10, 1.0
	v_fmac_f32_e32 v10, v12, v10
	v_mul_f32_e32 v12, v11, v10
	v_fma_f32 v13, -v9, v12, v11
	v_fmac_f32_e32 v12, v13, v10
	v_fma_f32 v9, -v9, v12, v11
	v_div_fmas_f32 v9, v9, v10, v12
	v_div_fixup_f32 v7, v9, v8, v7
	ds_write_b32 v6, v7
	v_add_u32_e32 v6, 0x800, v6
	s_waitcnt vmcnt(0)
	v_mov_b32_e32 v7, v21
	v_mul_f32_e32 v8, 0xbfb8aa3b, v7
	v_rndne_f32_e32 v9, v8
	v_fma_f32 v10, v7, s3, -v8
	v_sub_f32_e32 v8, v8, v9
	v_fmac_f32_e32 v10, 0xb2a5705f, v7
	v_add_f32_e32 v8, v8, v10
	v_cvt_i32_f32_e32 v9, v9
	v_exp_f32_e32 v8, v8
	v_cmp_nlt_f32_e32 vcc, s6, v7
	v_ldexp_f32 v8, v8, v9
	s_nop 0
	v_cndmask_b32_e32 v8, 0, v8, vcc
	v_cmp_ngt_f32_e32 vcc, s7, v7
	s_nop 1
	v_cndmask_b32_e32 v8, v3, v8, vcc
	v_add_f32_e32 v8, 1.0, v8
	v_div_scale_f32 v9, s[10:11], v8, v8, v7
	v_rcp_f32_e32 v10, v9
	v_div_scale_f32 v11, vcc, v7, v8, v7
	v_fma_f32 v12, -v9, v10, 1.0
	v_fmac_f32_e32 v10, v12, v10
	v_mul_f32_e32 v12, v11, v10
	v_fma_f32 v13, -v9, v12, v11
	v_fmac_f32_e32 v12, v13, v10
	v_fma_f32 v9, -v9, v12, v11
	v_div_fmas_f32 v9, v9, v10, v12
	v_div_fixup_f32 v7, v9, v8, v7
	ds_write_b32 v6, v7
	v_add_u32_e32 v6, 0x800, v6
	s_or_b64 exec, exec, s[0:1]
	v_lshrrev_b32_e32 v1, 6, v0
	v_and_b32_e32 v2, 0xfc, v2
	v_lshlrev_b32_e32 v3, 11, v1
	v_lshlrev_b32_e32 v4, 2, v2
	v_add3_u32 v24, 0, v3, v4
	v_lshrrev_b32_e32 v3, 8, v0
	v_and_b32_e32 v4, 0x100, v0
	v_mov_b32_e32 v5, 2
	v_readlane_b32 s4, v255, 0
	s_add_u32 s0, s74, 0x8000
	v_lshlrev_b32_e32 v4, 2, v4
	v_lshlrev_b32_sdwa v5, v5, v0 dst_sel:DWORD dst_unused:UNUSED_PAD src0_sel:DWORD src1_sel:BYTE_0
	v_mul_u32_u24_e32 v3, 0x3000, v3
	v_readlane_b32 s8, v255, 4
	v_readlane_b32 s9, v255, 5
	v_readlane_b32 s10, v255, 6
	v_readlane_b32 s11, v255, 7
	v_readlane_b32 s12, v255, 8
	v_readlane_b32 s13, v255, 9
	v_readlane_b32 s14, v255, 10
	v_readlane_b32 s15, v255, 11
	v_readlane_b32 s16, v255, 12
	v_readlane_b32 s17, v255, 13
	v_readlane_b32 s18, v255, 14
	v_readlane_b32 s19, v255, 15
	s_addc_u32 s1, s75, 0
	v_mov_b32_e32 v11, 0
	v_add3_u32 v25, 0, v4, v5
	v_or_b32_sdwa v26, v3, v0 dst_sel:DWORD dst_unused:UNUSED_PAD src0_sel:DWORD src1_sel:BYTE_0
	s_mov_b32 s3, 0xc000
	v_mov_b64_e32 v[12:13], s[8:9]
	v_lshlrev_b32_e32 v10, 2, v2
	s_mov_b32 s8, 0x60000
	s_mov_b32 s9, 0xc0000
	s_mov_b32 s10, 0x120000
	s_mov_b32 s11, 0x180000
	s_mov_b32 s12, 0x1e0000
	s_mov_b32 s13, 0x240000
	s_mov_b32 s14, 0x2a0000
	s_mov_b32 s15, 0x300000
	s_mov_b32 s16, 0x360000
	s_mov_b32 s17, 0x3c0000
	s_mov_b32 s18, 0x420000
	s_mov_b32 s19, 0x480000
	s_mov_b32 s20, 0x4e0000
	s_mov_b32 s21, 0x540000
	s_mov_b32 s22, 0x5a0000
	s_mov_b32 s23, s96
	s_waitcnt lgkmcnt(0)
	s_barrier
	v_readlane_b32 s5, v255, 1
	v_readlane_b32 s6, v255, 2
	v_readlane_b32 s7, v255, 3
	s_branch .LBB0_11
